# baseline (speedup 1.0000x reference)
.LBB3_16:
	s_or_b64 exec, exec, s[4:5]
	v_and_b32_e32 v92, 63, v0
	s_lshr_b32 s27, s26, 6
	v_lshlrev_b32_e32 v30, 2, v0
	v_mov_b32_e32 v31, -1
	v_mov_b32_e32 v34, 0
	v_cmp_gt_u32_e64 s[14:15], 12, v0
	s_and_saveexec_b64 s[16:17], s[14:15]
	ds_write_b32 v30, v31 offset:54144
	s_mov_b64 exec, s[16:17]
	s_waitcnt vmcnt(0)
	v_add_u32_e32 v42, v2, v3
	v_add_u32_e32 v52, v11, v5
	v_add_u32_e32 v43, v8, v42
	v_add_u32_e32 v53, v4, v52
	v_add_u32_e32 v44, v9, v43
	v_add_u32_e32 v54, v1, v53
	v_add_u32_e32 v45, v10, v44
	v_add_u32_e32 v55, v16, v54
	v_add_u32_e32 v46, v12, v45
	v_add_u32_e32 v56, v15, v55
	v_add_u32_e32 v47, v13, v46
	v_add_u32_e32 v57, v21, v56
	v_add_u32_e32 v48, v14, v47
	v_add_u32_e32 v58, v17, v57
	v_add_u32_e32 v49, 0x7f, v48
	v_add_u32_e32 v59, 0x7f, v58
	v_lshrrev_b32_e32 v49, 7, v49
	v_lshrrev_b32_e32 v59, 7, v59
	v_mov_b32_e32 v50, v49
	v_mov_b32_e32 v51, v59
	s_nop 0
	v_add_u32_dpp v50, v50, v50 row_shr:1 row_mask:0xf bank_mask:0xf
	v_add_u32_dpp v51, v51, v51 row_shr:1 row_mask:0xf bank_mask:0xf
	s_nop 0
	v_add_u32_dpp v50, v50, v50 row_shr:2 row_mask:0xf bank_mask:0xf
	v_add_u32_dpp v51, v51, v51 row_shr:2 row_mask:0xf bank_mask:0xf
	s_nop 0
	v_add_u32_dpp v50, v50, v50 row_shr:4 row_mask:0xf bank_mask:0xf
	v_add_u32_dpp v51, v51, v51 row_shr:4 row_mask:0xf bank_mask:0xf
	s_nop 0
	v_add_u32_dpp v50, v50, v50 row_shr:8 row_mask:0xf bank_mask:0xf
	v_add_u32_dpp v51, v51, v51 row_shr:8 row_mask:0xf bank_mask:0xf
	s_nop 0
	v_add_u32_dpp v50, v50, v50 row_bcast:15 row_mask:0xa bank_mask:0xf
	v_add_u32_dpp v51, v51, v51 row_bcast:15 row_mask:0xa bank_mask:0xf
	s_nop 0
	v_add_u32_dpp v50, v50, v50 row_bcast:31 row_mask:0xc bank_mask:0xf
	v_add_u32_dpp v51, v51, v51 row_bcast:31 row_mask:0xc bank_mask:0xf
	s_nop 0
	v_readlane_b32 s6, v50, 63
	s_lshl_b32 s7, s27, 2
	v_mov_b32_e32 v33, s7
	v_cmp_eq_u32_e64 s[14:15], 0, v92
	v_mov_b32_e32 v32, s6
	s_and_saveexec_b64 s[16:17], s[14:15]
	ds_write_b32 v33, v32 offset:54192
	s_mov_b64 exec, s[16:17]
	s_waitcnt lgkmcnt(0)
	s_barrier
	ds_read_b128 v[64:67], v34 offset:54192
	s_waitcnt lgkmcnt(0)
	v_readfirstlane_b32 s6, v64
	v_readfirstlane_b32 s7, v65
	v_readfirstlane_b32 s8, v66
	v_readfirstlane_b32 s9, v67
	s_nop 3
	s_add_u32 s10, s6, s7
	s_add_u32 s10, s10, s8
	s_add_u32 s10, s10, s9
	s_cmp_gt_u32 s27, 0
	s_cselect_b32 s14, s6, 0
	s_cmp_gt_u32 s27, 1
	s_cselect_b32 s15, s7, 0
	s_cmp_gt_u32 s27, 2
	s_cselect_b32 s16, s8, 0
	s_add_u32 s11, s14, s15
	s_add_u32 s11, s11, s16
	v_sub_u32_e32 v68, v50, v49
	v_sub_u32_e32 v69, v51, v59
	v_add_u32_e32 v68, s11, v68
	v_add_u32_e32 v69, s10, v69
	v_add_u32_e32 v70, v68, v49
	v_add_u32_e32 v71, v69, v59
	v_mov_b32_e32 v36, v0
	v_sub_u32_e32 v37, s2, v68
	v_mov_b32_e32 v38, v48
	v_mov_b32_e32 v39, v3
	v_or_b32_e32 v60, 0x100, v0
	v_sub_u32_e32 v61, s2, v69
	v_mov_b32_e32 v62, v58
	v_mov_b32_e32 v63, v5
	v_cmp_ge_u32_e64 s[14:15], s2, v68
	v_cmp_lt_u32_e64 s[16:17], s2, v70
	v_cmp_ge_u32_e64 s[6:7], s2, v69
	v_cmp_lt_u32_e64 s[8:9], s2, v71
	s_and_b64 s[14:15], s[14:15], s[16:17]
	s_and_b64 s[6:7], s[6:7], s[8:9]
	s_and_saveexec_b64 s[16:17], s[14:15]
	ds_write_b128 v34, v[36:39] offset:54144
	ds_write_b128 v34, v[42:45] offset:54160
	ds_write_b96 v34, v[46:48] offset:54176
	s_mov_b64 exec, s[16:17]
	s_and_saveexec_b64 s[16:17], s[6:7]
	ds_write_b128 v34, v[60:63] offset:54144
	ds_write_b128 v34, v[52:55] offset:54160
	ds_write_b96 v34, v[56:58] offset:54176
	s_mov_b64 exec, s[16:17]
	v_mov_b32_e32 v1, 0
	s_waitcnt lgkmcnt(0)
	s_barrier
	ds_read_b32 v2, v1 offset:54144
	s_waitcnt lgkmcnt(0)
	v_cmp_gt_i32_e32 vcc, 0, v2
	v_readfirstlane_b32 s2, v2
	s_cbranch_vccnz .LBB3_39
	v_mov_b32_e32 v5, 0xd39c
	v_mov_b32_e32 v2, 0xd384
	v_mov_b32_e32 v3, 0xd38c
	v_mov_b32_e32 v4, 0xd394
	ds_read2_b32 v[8:9], v5 offset1:1
	ds_read2_b32 v[6:7], v2 offset1:1
	ds_read2_b32 v[12:13], v3 offset1:1
	ds_read2_b32 v[10:11], v4 offset1:1
	ds_read_b32 v1, v1 offset:54180
	s_mov_b32 s28, 0
	s_add_u32 s1, s28, 16
	s_sub_u32 s3, 47, s1
	s_mul_i32 s3, s3, s1
	s_lshr_b32 s3, s3, 1
	s_cmp_ge_u32 s2, s3
	s_cselect_b32 s28, s1, s28
	s_add_u32 s1, s28, 8
	s_sub_u32 s3, 47, s1
	s_mul_i32 s3, s3, s1
	s_lshr_b32 s3, s3, 1
	s_cmp_ge_u32 s2, s3
	s_cselect_b32 s28, s1, s28
	s_add_u32 s1, s28, 4
	s_sub_u32 s3, 47, s1
	s_mul_i32 s3, s3, s1
	s_lshr_b32 s3, s3, 1
	s_cmp_ge_u32 s2, s3
	s_cselect_b32 s28, s1, s28
	s_add_u32 s1, s28, 2
	s_sub_u32 s3, 47, s1
	s_mul_i32 s3, s3, s1
	s_lshr_b32 s3, s3, 1
	s_cmp_ge_u32 s2, s3
	s_cselect_b32 s28, s1, s28
	s_add_u32 s1, s28, 1
	s_sub_u32 s3, 47, s1
	s_mul_i32 s3, s3, s1
	s_lshr_b32 s3, s3, 1
	s_cmp_ge_u32 s2, s3
	s_cselect_b32 s28, s1, s28
	s_sub_u32 s3, 47, s28
	s_mul_i32 s3, s3, s28
	s_lshr_b32 s3, s3, 1
	s_sub_u32 s0, s2, s3
	s_add_i32 s29, s28, s0
	s_add_i32 s29, s29, 1
	s_mul_hi_u32 s4, s2, 0x20680
	s_mul_i32 s5, s2, 0x20680
	v_lshrrev_b32_e32 v2, 6, v0
	s_movk_i32 s2, 0x180
	v_mov_b32_e32 v24, s29
	v_mov_b32_e32 v25, s28
	v_cmp_gt_u32_e32 vcc, s2, v0
	v_add_u32_e32 v4, -6, v2
	s_waitcnt lgkmcnt(0)
	v_lshlrev_b32_e32 v6, 7, v6
	v_cndmask_b32_e32 v3, v24, v25, vcc
	v_cndmask_b32_e32 v2, v4, v2, vcc
	v_mad_u64_u32 v[2:3], s[2:3], v3, 6, v[2:3]
	v_or_b32_e32 v4, 0x100, v0
	v_lshrrev_b32_e32 v4, 6, v4
	s_movk_i32 s2, 0x80
	v_cmp_gt_u32_e32 vcc, s2, v0
	v_add_u32_e32 v14, -6, v4
	s_lshl_b32 s0, s27, 5
	v_cndmask_b32_e32 v5, v24, v25, vcc
	v_cndmask_b32_e32 v4, v14, v4, vcc
	v_add_u32_e32 v36, s0, v6
	s_add_u32 s0, s20, 0x20000
	v_lshl_or_b32 v2, v2, 6, v92
	v_mad_u64_u32 v[4:5], s[2:3], v5, 6, v[4:5]
	s_addc_u32 s1, s21, 0
	v_ashrrev_i32_e32 v3, 31, v2
	v_lshl_or_b32 v4, v4, 6, v92
	v_lshl_add_u64 v[2:3], v[2:3], 4, s[0:1]
	v_ashrrev_i32_e32 v5, 31, v4
	v_lshl_add_u64 v[4:5], v[4:5], 4, s[0:1]
	global_load_dwordx4 v[16:19], v[2:3], off
	global_load_dwordx4 v[20:23], v[4:5], off
	v_or_b32_e32 v2, 0x200, v0
	v_lshrrev_b32_e32 v2, 6, v2
	v_mad_u64_u32 v[2:3], s[2:3], s29, 6, v[2:3]
	v_lshl_or_b32 v2, v2, 6, v92
	v_add_u32_e32 v14, 0xfffffe80, v2
	v_mov_b32_e32 v15, 0
	v_lshl_add_u64 v[28:29], v[14:15], 4, s[0:1]
	s_add_u32 s0, s20, s5
	v_min_u32_e32 v2, 47, v0
	s_addc_u32 s1, s21, s4
	v_cmp_gt_u32_e32 vcc, 24, v0
	v_subrev_u32_e32 v4, 24, v2
	s_add_u32 s24, s0, 0x800000
	v_cndmask_b32_e32 v3, v24, v25, vcc
	v_cndmask_b32_e32 v2, v4, v2, vcc
	s_addc_u32 s25, s1, 0
	v_mad_u64_u32 v[2:3], s[0:1], v3, 24, v[2:3]
	v_mov_b32_e32 v3, v15
	v_lshl_add_u64 v[2:3], v[2:3], 4, s[20:21]
	s_movk_i32 s0, 0x1000
	v_and_or_b32 v32, v0, 31, v36
	v_add_co_u32_e32 v30, vcc, s0, v2
	v_cmp_lt_i32_e64 s[0:1], v32, v7
	s_nop 0
	v_addc_co_u32_e32 v31, vcc, 0, v3, vcc
	v_cndmask_b32_e64 v14, v36, v32, s[0:1]
	v_cmp_lt_i32_e32 vcc, v36, v7
	global_load_dwordx4 v[24:27], v[28:29], off
	global_load_dwordx4 v[2:5], v[30:31], off
	v_cndmask_b32_e32 v14, v6, v14, vcc
	v_cmp_lt_i32_e64 s[2:3], v14, v12
	v_cmp_lt_i32_e64 s[4:5], v14, v13
	v_mov_b32_e32 v37, 0x1034
	v_cndmask_b32_e64 v28, v12, 0, s[2:3]
	v_cndmask_b32_e64 v28, v13, v28, s[4:5]
	v_cmp_lt_i32_e64 s[6:7], v14, v10
	v_cndmask_b32_e64 v29, v37, 0, s[2:3]
	v_mov_b32_e32 v38, 0x2068
	v_cndmask_b32_e64 v28, v10, v28, s[6:7]
	v_cmp_lt_i32_e64 s[8:9], v14, v11
	v_cndmask_b32_e64 v29, v38, v29, s[4:5]
	v_mov_b32_e32 v39, 0x309c
	v_cndmask_b32_e64 v28, v11, v28, s[8:9]
	v_cmp_lt_i32_e64 s[10:11], v14, v8
	v_cndmask_b32_e64 v29, v39, v29, s[6:7]
	v_mov_b32_e32 v40, 0x40d0
	v_cndmask_b32_e64 v28, v8, v28, s[10:11]
	v_cmp_lt_i32_e64 s[14:15], v14, v9
	v_cndmask_b32_e64 v29, v40, v29, s[8:9]
	v_mov_b32_e32 v41, 0x5104
	v_cndmask_b32_e64 v28, v9, v28, s[14:15]
	v_cmp_lt_i32_e64 s[16:17], v14, v1
	v_cndmask_b32_e64 v29, v41, v29, s[10:11]
	v_mov_b32_e32 v42, 0x6138
	v_cndmask_b32_e64 v28, v1, v28, s[16:17]
	v_cndmask_b32_e64 v29, v42, v29, s[14:15]
	v_mov_b32_e32 v43, 0x716c
	v_cndmask_b32_e64 v29, v43, v29, s[16:17]
	v_sub_u32_e32 v14, v14, v28
	v_add_u32_e32 v28, v14, v29
	v_lshrrev_b32_e32 v14, 3, v92
	v_or_b32_e32 v14, v36, v14
	v_cmp_lt_i32_e64 s[2:3], v14, v7
	v_ashrrev_i32_e32 v29, 31, v28
	v_lshl_add_u64 v[28:29], v[28:29], 2, s[24:25]
	v_cndmask_b32_e64 v30, v36, v14, s[2:3]
	v_cndmask_b32_e32 v30, v6, v30, vcc
	v_cmp_lt_i32_e64 s[2:3], v30, v12
	v_cmp_lt_i32_e64 s[4:5], v30, v13
	v_cmp_lt_i32_e64 s[6:7], v30, v10
	v_cndmask_b32_e64 v31, v12, 0, s[2:3]
	v_cndmask_b32_e64 v31, v13, v31, s[4:5]
	v_cndmask_b32_e64 v32, v37, 0, s[2:3]
	v_cndmask_b32_e64 v31, v10, v31, s[6:7]
	v_cmp_lt_i32_e64 s[8:9], v30, v11
	v_cndmask_b32_e64 v32, v38, v32, s[4:5]
	v_cmp_lt_i32_e64 s[10:11], v30, v8
	v_cndmask_b32_e64 v31, v11, v31, s[8:9]
	v_cndmask_b32_e64 v32, v39, v32, s[6:7]
	v_cndmask_b32_e64 v31, v8, v31, s[10:11]
	v_cmp_lt_i32_e64 s[14:15], v30, v9
	v_cndmask_b32_e64 v32, v40, v32, s[8:9]
	v_cmp_lt_i32_e64 s[16:17], v30, v1
	v_cndmask_b32_e64 v31, v9, v31, s[14:15]
	v_cndmask_b32_e64 v32, v41, v32, s[10:11]
	v_cndmask_b32_e64 v31, v1, v31, s[16:17]
	v_cndmask_b32_e64 v32, v42, v32, s[14:15]
	v_cndmask_b32_e64 v32, v43, v32, s[16:17]
	v_sub_u32_e32 v30, v30, v31
	v_add_u32_e32 v30, v30, v32
	v_or_b32_e32 v32, 8, v14
	v_cmp_lt_i32_e64 s[2:3], v32, v7
	v_ashrrev_i32_e32 v31, 31, v30
	v_lshl_add_u64 v[30:31], v[30:31], 2, s[24:25]
	v_cndmask_b32_e64 v32, v36, v32, s[2:3]
	v_cndmask_b32_e32 v32, v6, v32, vcc
	v_cmp_lt_i32_e64 s[2:3], v32, v12
	v_cmp_lt_i32_e64 s[4:5], v32, v13
	v_cmp_lt_i32_e64 s[6:7], v32, v10
	v_cndmask_b32_e64 v33, v12, 0, s[2:3]
	v_cndmask_b32_e64 v33, v13, v33, s[4:5]
	v_cndmask_b32_e64 v34, v37, 0, s[2:3]
	v_cndmask_b32_e64 v33, v10, v33, s[6:7]
	v_cmp_lt_i32_e64 s[8:9], v32, v11
	v_cndmask_b32_e64 v34, v38, v34, s[4:5]
	v_cmp_lt_i32_e64 s[10:11], v32, v8
	v_cndmask_b32_e64 v33, v11, v33, s[8:9]
	v_cndmask_b32_e64 v34, v39, v34, s[6:7]
	v_cndmask_b32_e64 v33, v8, v33, s[10:11]
	v_cmp_lt_i32_e64 s[14:15], v32, v9
	v_cndmask_b32_e64 v34, v40, v34, s[8:9]
	v_cmp_lt_i32_e64 s[16:17], v32, v1
	v_cndmask_b32_e64 v33, v9, v33, s[14:15]
	v_cndmask_b32_e64 v34, v41, v34, s[10:11]
	v_cndmask_b32_e64 v33, v1, v33, s[16:17]
	v_cndmask_b32_e64 v34, v42, v34, s[14:15]
	v_cndmask_b32_e64 v34, v43, v34, s[16:17]
	v_sub_u32_e32 v32, v32, v33
	v_add_u32_e32 v32, v32, v34
	v_or_b32_e32 v34, 16, v14
	v_cmp_lt_i32_e64 s[2:3], v34, v7
	v_or_b32_e32 v14, 24, v14
	v_ashrrev_i32_e32 v33, 31, v32
	v_cndmask_b32_e64 v34, v36, v34, s[2:3]
	v_cndmask_b32_e32 v34, v6, v34, vcc
	v_cmp_lt_i32_e64 s[2:3], v34, v12
	v_cmp_lt_i32_e64 s[4:5], v34, v13
	v_cmp_lt_i32_e64 s[6:7], v34, v10
	v_cndmask_b32_e64 v35, v12, 0, s[2:3]
	v_cndmask_b32_e64 v44, v37, 0, s[2:3]
	v_cmp_lt_i32_e64 s[2:3], v14, v7
	v_cndmask_b32_e64 v35, v13, v35, s[4:5]
	v_cndmask_b32_e64 v44, v38, v44, s[4:5]
	v_cndmask_b32_e64 v14, v36, v14, s[2:3]
	v_cndmask_b32_e32 v6, v6, v14, vcc
	v_cmp_lt_i32_e32 vcc, v6, v12
	v_cmp_lt_i32_e64 s[2:3], v6, v13
	v_cmp_lt_i32_e64 s[4:5], v6, v10
	v_cndmask_b32_e64 v12, v12, 0, vcc
	v_cndmask_b32_e64 v12, v13, v12, s[2:3]
	v_cndmask_b32_e64 v35, v10, v35, s[6:7]
	v_cmp_lt_i32_e64 s[8:9], v34, v11
	v_cndmask_b32_e64 v44, v39, v44, s[6:7]
	v_cndmask_b32_e64 v10, v10, v12, s[4:5]
	v_cmp_lt_i32_e64 s[6:7], v6, v11
	v_cndmask_b32_e64 v35, v11, v35, s[8:9]
	v_cmp_lt_i32_e64 s[10:11], v34, v8
	v_cndmask_b32_e64 v44, v40, v44, s[8:9]
	v_cndmask_b32_e64 v10, v11, v10, s[6:7]
	v_cmp_lt_i32_e64 s[8:9], v6, v8
	v_cndmask_b32_e64 v35, v8, v35, s[10:11]
	v_cmp_lt_i32_e64 s[14:15], v34, v9
	v_cndmask_b32_e64 v44, v41, v44, s[10:11]
	v_cndmask_b32_e64 v8, v8, v10, s[8:9]
	v_cmp_lt_i32_e64 s[10:11], v6, v9
	v_cndmask_b32_e64 v35, v9, v35, s[14:15]
	v_cmp_lt_i32_e64 s[16:17], v34, v1
	v_cndmask_b32_e64 v44, v42, v44, s[14:15]
	v_cndmask_b32_e64 v8, v9, v8, s[10:11]
	v_cmp_lt_i32_e64 s[14:15], v6, v1
	v_cndmask_b32_e64 v35, v1, v35, s[16:17]
	v_cndmask_b32_e64 v44, v43, v44, s[16:17]
	v_cndmask_b32_e64 v1, v1, v8, s[14:15]
	v_cndmask_b32_e64 v8, v37, 0, vcc
	v_cndmask_b32_e64 v8, v38, v8, s[2:3]
	v_cndmask_b32_e64 v8, v39, v8, s[4:5]
	v_cndmask_b32_e64 v8, v40, v8, s[6:7]
	v_cndmask_b32_e64 v8, v41, v8, s[8:9]
	v_cndmask_b32_e64 v8, v42, v8, s[10:11]
	v_sub_u32_e32 v34, v34, v35
	v_cndmask_b32_e64 v8, v43, v8, s[14:15]
	v_sub_u32_e32 v1, v6, v1
	v_add_u32_e32 v34, v34, v44
	v_add_u32_e32 v8, v1, v8
	v_ashrrev_i32_e32 v35, 31, v34
	v_ashrrev_i32_e32 v9, 31, v8
	v_lshl_add_u64 v[32:33], v[32:33], 2, s[24:25]
	v_lshl_add_u64 v[34:35], v[34:35], 2, s[24:25]
	v_lshl_add_u64 v[10:11], v[8:9], 2, s[24:25]
	global_load_dword v80, v[28:29], off
	global_load_dword v9, v[30:31], off
	global_load_dword v8, v[32:33], off
	global_load_dword v6, v[34:35], off
	global_load_dword v1, v[10:11], off
	v_cmp_ge_i32_e32 vcc, v36, v7
	v_lshlrev_b32_e32 v7, 4, v0
	s_waitcnt vmcnt(8)
	ds_write_b128 v7, v[16:19] offset:40960
	s_waitcnt vmcnt(7)
	ds_write_b128 v7, v[20:23] offset:45056
	s_waitcnt vmcnt(6)
	ds_write_b128 v7, v[24:27] offset:49152
	s_and_saveexec_b64 s[4:5], s[12:13]
	s_cbranch_execz .LBB3_31
	v_min_u32_e32 v10, 19, v0
	v_mov_b32_e32 v11, s29
	v_mov_b32_e32 v12, s28
	v_cmp_gt_u32_e64 s[2:3], 10, v0
	s_nop 1
	v_cndmask_b32_e64 v11, v11, v12, s[2:3]
	v_add_u32_e32 v12, -10, v10
	v_cndmask_b32_e64 v10, v12, v10, s[2:3]
	v_mad_u64_u32 v[10:11], s[2:3], v11, 10, v[10:11]
	v_mov_b32_e32 v11, v15
	v_lshl_add_u64 v[10:11], v[10:11], 2, s[22:23]
	global_load_dword v10, v[10:11], off
	v_mov_b32_e32 v11, 0xd300
	v_mov_b32_e32 v12, 0xd340
	v_cmp_lt_u32_e64 s[2:3], 9, v0
	s_nop 1
	v_cndmask_b32_e64 v11, v11, v12, s[2:3]
	v_add_u32_e32 v12, -10, v0
	v_min_u32_e32 v12, v0, v12
	v_lshl_add_u32 v11, v12, 2, v11
	s_waitcnt vmcnt(0)
	ds_write_b32 v11, v10
